# v52 with the atomics wait + ELL stores deferred from before barrier 0 to loader step 4 (counted vmcnt)
# speedup vs baseline: 1.0139x; 1.0139x over previous
.LBB1_248:
	v_and_b32_e32 v6, 31, v0
	v_bfe_u32 v7, v0, 5, 3
	s_cmp_lt_u32 s8, 0x2000
	s_cselect_b32 s50, s12, s14
	s_cselect_b32 s51, s13, s15
	s_and_b32 s0, s8, 0x1fff
	s_mul_i32 s1, s0, 0x2ee0
	s_add_u32 s50, s50, s1
	s_addc_u32 s51, s51, 0
	s_mov_b32 s52, s50
	s_mov_b32 s53, s51
	s_add_u32 s54, s50, 0x17700
	s_addc_u32 s55, s51, 0
	s_add_u32 s56, s50, 0x2ee00
	s_addc_u32 s57, s51, 0
	s_add_u32 s58, s50, 0x46500
	s_addc_u32 s59, s51, 0
	s_add_u32 s60, s50, 0x5dc00
	s_addc_u32 s61, s51, 0
	s_add_u32 s62, s50, 0x75300
	s_addc_u32 s63, s51, 0
	s_add_u32 s64, s50, 0x8ca00
	s_addc_u32 s65, s51, 0
	s_add_u32 s66, s50, 0xa4100
	s_addc_u32 s67, s51, 0
	v_and_b32_e32 v136, 3, v7
	v_lshl_add_u32 v137, v136, 1, v6
	s_movk_i32 s0, 0x2ee0
	v_mul_lo_u32 v2, v7, s0
	v_lshl_add_u32 v2, v137, 4, v2
	s_movk_i32 s0, 0x110
	v_mul_lo_u32 v3, v7, s0
	v_lshl_add_u32 v138, v137, 3, v3
	v_cmp_le_u32_e64 s[76:77], 32, v137
	v_cmp_gt_u32_e64 s[68:69], 14, v137
	s_not_b64 s[78:79], s[76:77]
	v_mov_b32_e32 v139, 0x0
	v_mov_b32_e32 v140, 0x4300
	v_cndmask_b32_e64 v139, v139, v140, s[76:77]
	v_add_u32_e32 v141, v138, v139
	v_mov_b32_e32 v139, 0x4400
	v_mov_b32_e32 v140, 0x8700
	v_cndmask_b32_e64 v139, v139, v140, s[76:77]
	v_add_u32_e32 v142, v138, v139
	v_mov_b32_e32 v139, 0x8800
	v_mov_b32_e32 v140, 0xcb00
	v_cndmask_b32_e64 v139, v139, v140, s[76:77]
	v_add_u32_e32 v143, v138, v139
	v_mov_b32_e32 v139, 0xcc00
	v_mov_b32_e32 v140, 0xffffff00
	v_cndmask_b32_e64 v139, v139, v140, s[76:77]
	v_add_u32_e32 v144, v138, v139
	s_add_u32 s48, s18, 0x100000
	s_addc_u32 s49, s19, 0
	s_lshl_b32 s0, s10, 12
	v_add_u32_e32 v150, 0xfffffe00, v0
	v_lshl_add_u32 v150, v150, 4, s0
	global_load_dwordx4 v[152:155], v150, s[48:49]
	global_load_dwordx4 v[156:159], v150, s[18:19]
	v_mov_b32_e32 v104, 0
	v_mov_b32_e32 v105, 0
	v_mov_b32_e32 v106, 0
	v_mov_b32_e32 v107, 0
	s_mov_b64 s[70:71], exec
	s_mov_b64 exec, s[76:77]
	global_load_dwordx4 v[104:107], v2, s[52:53] offset:-512 sc1 nt
	s_mov_b64 exec, s[70:71]
	v_mov_b32_e32 v108, 0
	v_mov_b32_e32 v109, 0
	v_mov_b32_e32 v110, 0
	v_mov_b32_e32 v111, 0
	s_mov_b64 s[70:71], exec
	s_mov_b64 exec, s[76:77]
	global_load_dwordx4 v[108:111], v2, s[54:55] offset:-512 sc1 nt
	s_mov_b64 exec, s[70:71]
	v_mov_b32_e32 v112, 0
	v_mov_b32_e32 v113, 0
	v_mov_b32_e32 v114, 0
	v_mov_b32_e32 v115, 0
	s_mov_b64 s[70:71], exec
	s_mov_b64 exec, s[76:77]
	global_load_dwordx4 v[112:115], v2, s[56:57] offset:-512 sc1 nt
	s_mov_b64 exec, s[70:71]
	v_mov_b32_e32 v116, 0
	v_mov_b32_e32 v117, 0
	v_mov_b32_e32 v118, 0
	v_mov_b32_e32 v119, 0
	s_mov_b64 s[70:71], exec
	s_mov_b64 exec, s[76:77]
	global_load_dwordx4 v[116:119], v2, s[58:59] offset:-512 sc1 nt
	s_mov_b64 exec, s[70:71]
	v_mov_b32_e32 v120, 0
	v_mov_b32_e32 v121, 0
	v_mov_b32_e32 v122, 0
	v_mov_b32_e32 v123, 0
	s_mov_b64 s[70:71], exec
	s_mov_b64 exec, s[76:77]
	global_load_dwordx4 v[120:123], v2, s[60:61] offset:-512 sc1 nt
	s_mov_b64 exec, s[70:71]
	v_mov_b32_e32 v124, 0
	v_mov_b32_e32 v125, 0
	v_mov_b32_e32 v126, 0
	v_mov_b32_e32 v127, 0
	s_mov_b64 s[70:71], exec
	s_mov_b64 exec, s[76:77]
	global_load_dwordx4 v[124:127], v2, s[62:63] offset:-512 sc1 nt
	s_mov_b64 exec, s[70:71]
	v_mov_b32_e32 v128, 0
	v_mov_b32_e32 v129, 0
	v_mov_b32_e32 v130, 0
	v_mov_b32_e32 v131, 0
	s_mov_b64 s[70:71], exec
	s_mov_b64 exec, s[76:77]
	global_load_dwordx4 v[128:131], v2, s[64:65] offset:-512 sc1 nt
	s_mov_b64 exec, s[70:71]
	v_mov_b32_e32 v132, 0
	v_mov_b32_e32 v133, 0
	v_mov_b32_e32 v134, 0
	v_mov_b32_e32 v135, 0
	s_mov_b64 s[70:71], exec
	s_mov_b64 exec, s[76:77]
	global_load_dwordx4 v[132:135], v2, s[66:67] offset:-512 sc1 nt
	s_mov_b64 exec, s[70:71]
	global_load_dwordx4 v[8:11], v2, s[52:53] sc1 nt
	global_load_dwordx4 v[12:15], v2, s[54:55] sc1 nt
	global_load_dwordx4 v[16:19], v2, s[56:57] sc1 nt
	global_load_dwordx4 v[20:23], v2, s[58:59] sc1 nt
	global_load_dwordx4 v[24:27], v2, s[60:61] sc1 nt
	global_load_dwordx4 v[28:31], v2, s[62:63] sc1 nt
	global_load_dwordx4 v[32:35], v2, s[64:65] sc1 nt
	global_load_dwordx4 v[36:39], v2, s[66:67] sc1 nt
	global_load_dwordx4 v[40:43], v2, s[52:53] offset:512 sc1 nt
	global_load_dwordx4 v[44:47], v2, s[54:55] offset:512 sc1 nt
	global_load_dwordx4 v[48:51], v2, s[56:57] offset:512 sc1 nt
	global_load_dwordx4 v[52:55], v2, s[58:59] offset:512 sc1 nt
	global_load_dwordx4 v[56:59], v2, s[60:61] offset:512 sc1 nt
	global_load_dwordx4 v[60:63], v2, s[62:63] offset:512 sc1 nt
	global_load_dwordx4 v[64:67], v2, s[64:65] offset:512 sc1 nt
	global_load_dwordx4 v[68:71], v2, s[66:67] offset:512 sc1 nt
	global_load_dwordx4 v[72:75], v2, s[52:53] offset:1024 sc1 nt
	global_load_dwordx4 v[76:79], v2, s[54:55] offset:1024 sc1 nt
	global_load_dwordx4 v[80:83], v2, s[56:57] offset:1024 sc1 nt
	global_load_dwordx4 v[84:87], v2, s[58:59] offset:1024 sc1 nt
	global_load_dwordx4 v[88:91], v2, s[60:61] offset:1024 sc1 nt
	global_load_dwordx4 v[92:95], v2, s[62:63] offset:1024 sc1 nt
	global_load_dwordx4 v[96:99], v2, s[64:65] offset:1024 sc1 nt
	global_load_dwordx4 v[100:103], v2, s[66:67] offset:1024 sc1 nt
	s_waitcnt vmcnt(31)
	v_cvt_pk_f16_f32 v4, v104, v105
	v_cvt_pk_f16_f32 v5, v106, v107
	s_mov_b64 s[70:71], exec
	s_mov_b64 exec, s[76:77]
	ds_write_b64 v144, v[4:5]
	s_mov_b64 exec, s[70:71]
	global_load_dwordx4 v[104:107], v2, s[52:53] offset:1536 sc1 nt
	s_waitcnt vmcnt(31)
	v_cvt_pk_f16_f32 v4, v108, v109
	v_cvt_pk_f16_f32 v5, v110, v111
	s_mov_b64 s[70:71], exec
	s_mov_b64 exec, s[76:77]
	ds_write_b64 v144, v[4:5] offset:2176
	s_mov_b64 exec, s[70:71]
	global_load_dwordx4 v[108:111], v2, s[54:55] offset:1536 sc1 nt
	s_waitcnt vmcnt(31)
	v_cvt_pk_f16_f32 v4, v112, v113
	v_cvt_pk_f16_f32 v5, v114, v115
	s_mov_b64 s[70:71], exec
	s_mov_b64 exec, s[76:77]
	ds_write_b64 v144, v[4:5] offset:4352
	s_mov_b64 exec, s[70:71]
	global_load_dwordx4 v[112:115], v2, s[56:57] offset:1536 sc1 nt
	s_waitcnt vmcnt(31)
	v_cvt_pk_f16_f32 v4, v116, v117
	v_cvt_pk_f16_f32 v5, v118, v119
	s_mov_b64 s[70:71], exec
	s_mov_b64 exec, s[76:77]
	ds_write_b64 v144, v[4:5] offset:6528
	s_mov_b64 exec, s[70:71]
	global_load_dwordx4 v[116:119], v2, s[58:59] offset:1536 sc1 nt
	s_waitcnt vmcnt(31)
	v_cvt_pk_f16_f32 v4, v120, v121
	v_cvt_pk_f16_f32 v5, v122, v123
	s_mov_b64 s[70:71], exec
	s_mov_b64 exec, s[76:77]
	ds_write_b64 v144, v[4:5] offset:8704
	s_mov_b64 exec, s[70:71]
	global_load_dwordx4 v[120:123], v2, s[60:61] offset:1536 sc1 nt
	s_waitcnt vmcnt(31)
	v_cvt_pk_f16_f32 v4, v124, v125
	v_cvt_pk_f16_f32 v5, v126, v127
	s_mov_b64 s[70:71], exec
	s_mov_b64 exec, s[76:77]
	ds_write_b64 v144, v[4:5] offset:10880
	s_mov_b64 exec, s[70:71]
	global_load_dwordx4 v[124:127], v2, s[62:63] offset:1536 sc1 nt
	s_waitcnt vmcnt(31)
	v_cvt_pk_f16_f32 v4, v128, v129
	v_cvt_pk_f16_f32 v5, v130, v131
	s_mov_b64 s[70:71], exec
	s_mov_b64 exec, s[76:77]
	ds_write_b64 v144, v[4:5] offset:13056
	s_mov_b64 exec, s[70:71]
	global_load_dwordx4 v[128:131], v2, s[64:65] offset:1536 sc1 nt
	s_waitcnt vmcnt(31)
	v_cvt_pk_f16_f32 v4, v132, v133
	v_cvt_pk_f16_f32 v5, v134, v135
	s_mov_b64 s[70:71], exec
	s_mov_b64 exec, s[76:77]
	ds_write_b64 v144, v[4:5] offset:15232
	s_mov_b64 exec, s[70:71]
	global_load_dwordx4 v[132:135], v2, s[66:67] offset:1536 sc1 nt
	s_waitcnt vmcnt(40)
	v_mov_b32_e32 v151, 1
	v_lshlrev_b32_e32 v160, 2, v152
	v_lshlrev_b32_e32 v161, 2, v153
	v_lshlrev_b32_e32 v162, 2, v154
	v_lshlrev_b32_e32 v163, 2, v155
	global_atomic_add v164, v160, v151, s[20:21] sc0
	global_atomic_add v165, v161, v151, s[20:21] sc0
	global_atomic_add v166, v162, v151, s[20:21] sc0
	global_atomic_add v167, v163, v151, s[20:21] sc0
	s_waitcnt vmcnt(35)
	v_cvt_pk_f16_f32 v4, v8, v9
	v_cvt_pk_f16_f32 v5, v10, v11
	ds_write_b64 v141, v[4:5]
	s_waitcnt vmcnt(27)
	v_cvt_pk_f16_f32 v4, v40, v41
	v_cvt_pk_f16_f32 v5, v42, v43
	ds_write_b64 v142, v[4:5]
	global_load_dwordx4 v[8:11], v2, s[52:53] offset:2048 sc1 nt
	global_load_dwordx4 v[40:43], v2, s[52:53] offset:2560 sc1 nt
	s_waitcnt vmcnt(36)
	v_cvt_pk_f16_f32 v4, v12, v13
	v_cvt_pk_f16_f32 v5, v14, v15
	ds_write_b64 v141, v[4:5] offset:2176
	s_waitcnt vmcnt(28)
	v_cvt_pk_f16_f32 v4, v44, v45
	v_cvt_pk_f16_f32 v5, v46, v47
	ds_write_b64 v142, v[4:5] offset:2176
	global_load_dwordx4 v[12:15], v2, s[54:55] offset:2048 sc1 nt
	global_load_dwordx4 v[44:47], v2, s[54:55] offset:2560 sc1 nt
	s_waitcnt vmcnt(37)
	v_cvt_pk_f16_f32 v4, v16, v17
	v_cvt_pk_f16_f32 v5, v18, v19
	ds_write_b64 v141, v[4:5] offset:4352
	s_waitcnt vmcnt(29)
	v_cvt_pk_f16_f32 v4, v48, v49
	v_cvt_pk_f16_f32 v5, v50, v51
	ds_write_b64 v142, v[4:5] offset:4352
	global_load_dwordx4 v[16:19], v2, s[56:57] offset:2048 sc1 nt
	global_load_dwordx4 v[48:51], v2, s[56:57] offset:2560 sc1 nt
	s_waitcnt vmcnt(38)
	v_cvt_pk_f16_f32 v4, v20, v21
	v_cvt_pk_f16_f32 v5, v22, v23
	ds_write_b64 v141, v[4:5] offset:6528
	s_waitcnt vmcnt(30)
	v_cvt_pk_f16_f32 v4, v52, v53
	v_cvt_pk_f16_f32 v5, v54, v55
	ds_write_b64 v142, v[4:5] offset:6528
	global_load_dwordx4 v[20:23], v2, s[58:59] offset:2048 sc1 nt
	global_load_dwordx4 v[52:55], v2, s[58:59] offset:2560 sc1 nt
	s_waitcnt vmcnt(39)
	v_cvt_pk_f16_f32 v4, v24, v25
	v_cvt_pk_f16_f32 v5, v26, v27
	ds_write_b64 v141, v[4:5] offset:8704
	s_waitcnt vmcnt(31)
	v_cvt_pk_f16_f32 v4, v56, v57
	v_cvt_pk_f16_f32 v5, v58, v59
	ds_write_b64 v142, v[4:5] offset:8704
	global_load_dwordx4 v[24:27], v2, s[60:61] offset:2048 sc1 nt
	global_load_dwordx4 v[56:59], v2, s[60:61] offset:2560 sc1 nt
	s_waitcnt vmcnt(40)
	v_cvt_pk_f16_f32 v4, v28, v29
	v_cvt_pk_f16_f32 v5, v30, v31
	ds_write_b64 v141, v[4:5] offset:10880
	s_waitcnt vmcnt(32)
	v_cvt_pk_f16_f32 v4, v60, v61
	v_cvt_pk_f16_f32 v5, v62, v63
	ds_write_b64 v142, v[4:5] offset:10880
	global_load_dwordx4 v[28:31], v2, s[62:63] offset:2048 sc1 nt
	global_load_dwordx4 v[60:63], v2, s[62:63] offset:2560 sc1 nt
	s_waitcnt vmcnt(41)
	v_cvt_pk_f16_f32 v4, v32, v33
	v_cvt_pk_f16_f32 v5, v34, v35
	ds_write_b64 v141, v[4:5] offset:13056
	s_waitcnt vmcnt(33)
	v_cvt_pk_f16_f32 v4, v64, v65
	v_cvt_pk_f16_f32 v5, v66, v67
	ds_write_b64 v142, v[4:5] offset:13056
	global_load_dwordx4 v[32:35], v2, s[64:65] offset:2048 sc1 nt
	global_load_dwordx4 v[64:67], v2, s[64:65] offset:2560 sc1 nt
	s_waitcnt vmcnt(42)
	v_cvt_pk_f16_f32 v4, v36, v37
	v_cvt_pk_f16_f32 v5, v38, v39
	ds_write_b64 v141, v[4:5] offset:15232
	s_waitcnt vmcnt(34)
	v_cvt_pk_f16_f32 v4, v68, v69
	v_cvt_pk_f16_f32 v5, v70, v71
	ds_write_b64 v142, v[4:5] offset:15232
	global_load_dwordx4 v[36:39], v2, s[66:67] offset:2048 sc1 nt
	global_load_dwordx4 v[68:71], v2, s[66:67] offset:2560 sc1 nt
	s_waitcnt lgkmcnt(0)
	s_barrier
	s_waitcnt lgkmcnt(0)
	s_barrier
	s_waitcnt vmcnt(35)
	v_cvt_pk_f16_f32 v4, v72, v73
	v_cvt_pk_f16_f32 v5, v74, v75
	ds_write_b64 v143, v[4:5]
	s_waitcnt vmcnt(27)
	v_cvt_pk_f16_f32 v4, v104, v105
	v_cvt_pk_f16_f32 v5, v106, v107
	ds_write_b64 v144, v[4:5]
	global_load_dwordx4 v[72:75], v2, s[52:53] offset:3072 sc1 nt
	global_load_dwordx4 v[104:107], v2, s[52:53] offset:3584 sc1 nt
	s_waitcnt vmcnt(36)
	v_cvt_pk_f16_f32 v4, v76, v77
	v_cvt_pk_f16_f32 v5, v78, v79
	ds_write_b64 v143, v[4:5] offset:2176
	s_waitcnt vmcnt(28)
	v_cvt_pk_f16_f32 v4, v108, v109
	v_cvt_pk_f16_f32 v5, v110, v111
	ds_write_b64 v144, v[4:5] offset:2176
	global_load_dwordx4 v[76:79], v2, s[54:55] offset:3072 sc1 nt
	global_load_dwordx4 v[108:111], v2, s[54:55] offset:3584 sc1 nt
	s_waitcnt vmcnt(37)
	v_cvt_pk_f16_f32 v4, v80, v81
	v_cvt_pk_f16_f32 v5, v82, v83
	ds_write_b64 v143, v[4:5] offset:4352
	s_waitcnt vmcnt(29)
	v_cvt_pk_f16_f32 v4, v112, v113
	v_cvt_pk_f16_f32 v5, v114, v115
	ds_write_b64 v144, v[4:5] offset:4352
	global_load_dwordx4 v[80:83], v2, s[56:57] offset:3072 sc1 nt
	global_load_dwordx4 v[112:115], v2, s[56:57] offset:3584 sc1 nt
	s_waitcnt vmcnt(38)
	v_cvt_pk_f16_f32 v4, v84, v85
	v_cvt_pk_f16_f32 v5, v86, v87
	ds_write_b64 v143, v[4:5] offset:6528
	s_waitcnt vmcnt(30)
	v_cvt_pk_f16_f32 v4, v116, v117
	v_cvt_pk_f16_f32 v5, v118, v119
	ds_write_b64 v144, v[4:5] offset:6528
	global_load_dwordx4 v[84:87], v2, s[58:59] offset:3072 sc1 nt
	global_load_dwordx4 v[116:119], v2, s[58:59] offset:3584 sc1 nt
	s_waitcnt vmcnt(39)
	v_cvt_pk_f16_f32 v4, v88, v89
	v_cvt_pk_f16_f32 v5, v90, v91
	ds_write_b64 v143, v[4:5] offset:8704
	s_waitcnt vmcnt(31)
	v_cvt_pk_f16_f32 v4, v120, v121
	v_cvt_pk_f16_f32 v5, v122, v123
	ds_write_b64 v144, v[4:5] offset:8704
	global_load_dwordx4 v[88:91], v2, s[60:61] offset:3072 sc1 nt
	global_load_dwordx4 v[120:123], v2, s[60:61] offset:3584 sc1 nt
	s_waitcnt vmcnt(40)
	v_cvt_pk_f16_f32 v4, v92, v93
	v_cvt_pk_f16_f32 v5, v94, v95
	ds_write_b64 v143, v[4:5] offset:10880
	s_waitcnt vmcnt(32)
	v_cvt_pk_f16_f32 v4, v124, v125
	v_cvt_pk_f16_f32 v5, v126, v127
	ds_write_b64 v144, v[4:5] offset:10880
	global_load_dwordx4 v[92:95], v2, s[62:63] offset:3072 sc1 nt
	global_load_dwordx4 v[124:127], v2, s[62:63] offset:3584 sc1 nt
	s_waitcnt vmcnt(41)
	v_cvt_pk_f16_f32 v4, v96, v97
	v_cvt_pk_f16_f32 v5, v98, v99
	ds_write_b64 v143, v[4:5] offset:13056
	s_waitcnt vmcnt(33)
	v_cvt_pk_f16_f32 v4, v128, v129
	v_cvt_pk_f16_f32 v5, v130, v131
	ds_write_b64 v144, v[4:5] offset:13056
	global_load_dwordx4 v[96:99], v2, s[64:65] offset:3072 sc1 nt
	global_load_dwordx4 v[128:131], v2, s[64:65] offset:3584 sc1 nt
	s_waitcnt vmcnt(42)
	v_cvt_pk_f16_f32 v4, v100, v101
	v_cvt_pk_f16_f32 v5, v102, v103
	ds_write_b64 v143, v[4:5] offset:15232
	s_waitcnt vmcnt(34)
	v_cvt_pk_f16_f32 v4, v132, v133
	v_cvt_pk_f16_f32 v5, v134, v135
	ds_write_b64 v144, v[4:5] offset:15232
	global_load_dwordx4 v[100:103], v2, s[66:67] offset:3072 sc1 nt
	global_load_dwordx4 v[132:135], v2, s[66:67] offset:3584 sc1 nt
	s_waitcnt lgkmcnt(0)
	s_barrier
	s_waitcnt lgkmcnt(0)
	s_barrier
	s_waitcnt vmcnt(32)
	v_cmp_gt_i32_e32 vcc, 64, v164
	v_lshl_add_u32 v148, v152, 6, v164
	v_lshlrev_b32_e32 v148, 2, v148
	s_and_saveexec_b64 s[2:3], vcc
	global_store_dword v148, v156, s[22:23]
	s_xor_b64 exec, exec, s[2:3]
	s_cbranch_execz .Lg1_ld_ok_0
	v_mov_b32_e32 v149, 0x8000
	global_atomic_add v149, v149, v151, s[20:21] sc0
	s_waitcnt vmcnt(0)
	v_lshlrev_b32_e32 v149, 3, v149
	v_mov_b32_e32 v160, v152
	v_mov_b32_e32 v161, v156
	global_store_dwordx2 v149, v[160:161], s[28:29]

.Lg1_ld_ok_3:
	s_mov_b64 exec, -1
	s_waitcnt vmcnt(31)
	v_cvt_pk_f16_f32 v4, v8, v9
	v_cvt_pk_f16_f32 v5, v10, v11
	ds_write_b64 v141, v[4:5]
	s_waitcnt vmcnt(30)
	v_cvt_pk_f16_f32 v4, v40, v41
	v_cvt_pk_f16_f32 v5, v42, v43
	ds_write_b64 v142, v[4:5]
	v_add_u32_e32 v2, 0x1000, v2
	global_load_dwordx4 v[8:11], v2, s[52:53] sc1 nt
	global_load_dwordx4 v[40:43], v2, s[52:53] offset:512 sc1 nt
	s_waitcnt vmcnt(31)
	v_cvt_pk_f16_f32 v4, v12, v13
	v_cvt_pk_f16_f32 v5, v14, v15
	ds_write_b64 v141, v[4:5] offset:2176
	s_waitcnt vmcnt(30)
	v_cvt_pk_f16_f32 v4, v44, v45
	v_cvt_pk_f16_f32 v5, v46, v47
	ds_write_b64 v142, v[4:5] offset:2176
	global_load_dwordx4 v[12:15], v2, s[54:55] sc1 nt
	global_load_dwordx4 v[44:47], v2, s[54:55] offset:512 sc1 nt
	s_waitcnt vmcnt(31)
	v_cvt_pk_f16_f32 v4, v16, v17
	v_cvt_pk_f16_f32 v5, v18, v19
	ds_write_b64 v141, v[4:5] offset:4352
	s_waitcnt vmcnt(30)
	v_cvt_pk_f16_f32 v4, v48, v49
	v_cvt_pk_f16_f32 v5, v50, v51
	ds_write_b64 v142, v[4:5] offset:4352
	global_load_dwordx4 v[16:19], v2, s[56:57] sc1 nt
	global_load_dwordx4 v[48:51], v2, s[56:57] offset:512 sc1 nt
	s_waitcnt vmcnt(31)
	v_cvt_pk_f16_f32 v4, v20, v21
	v_cvt_pk_f16_f32 v5, v22, v23
	ds_write_b64 v141, v[4:5] offset:6528
	s_waitcnt vmcnt(30)
	v_cvt_pk_f16_f32 v4, v52, v53
	v_cvt_pk_f16_f32 v5, v54, v55
	ds_write_b64 v142, v[4:5] offset:6528
	global_load_dwordx4 v[20:23], v2, s[58:59] sc1 nt
	global_load_dwordx4 v[52:55], v2, s[58:59] offset:512 sc1 nt
	s_waitcnt vmcnt(31)
	v_cvt_pk_f16_f32 v4, v24, v25
	v_cvt_pk_f16_f32 v5, v26, v27
	ds_write_b64 v141, v[4:5] offset:8704
	s_waitcnt vmcnt(30)
	v_cvt_pk_f16_f32 v4, v56, v57
	v_cvt_pk_f16_f32 v5, v58, v59
	ds_write_b64 v142, v[4:5] offset:8704
	global_load_dwordx4 v[24:27], v2, s[60:61] sc1 nt
	global_load_dwordx4 v[56:59], v2, s[60:61] offset:512 sc1 nt
	s_waitcnt vmcnt(31)
	v_cvt_pk_f16_f32 v4, v28, v29
	v_cvt_pk_f16_f32 v5, v30, v31
	ds_write_b64 v141, v[4:5] offset:10880
	s_waitcnt vmcnt(30)
	v_cvt_pk_f16_f32 v4, v60, v61
	v_cvt_pk_f16_f32 v5, v62, v63
	ds_write_b64 v142, v[4:5] offset:10880
	global_load_dwordx4 v[28:31], v2, s[62:63] sc1 nt
	global_load_dwordx4 v[60:63], v2, s[62:63] offset:512 sc1 nt
	s_waitcnt vmcnt(31)
	v_cvt_pk_f16_f32 v4, v32, v33
	v_cvt_pk_f16_f32 v5, v34, v35
	ds_write_b64 v141, v[4:5] offset:13056
	s_waitcnt vmcnt(30)
	v_cvt_pk_f16_f32 v4, v64, v65
	v_cvt_pk_f16_f32 v5, v66, v67
	ds_write_b64 v142, v[4:5] offset:13056
	global_load_dwordx4 v[32:35], v2, s[64:65] sc1 nt
	global_load_dwordx4 v[64:67], v2, s[64:65] offset:512 sc1 nt
	s_waitcnt vmcnt(31)
	v_cvt_pk_f16_f32 v4, v36, v37
	v_cvt_pk_f16_f32 v5, v38, v39
	ds_write_b64 v141, v[4:5] offset:15232
	s_waitcnt vmcnt(30)
	v_cvt_pk_f16_f32 v4, v68, v69
	v_cvt_pk_f16_f32 v5, v70, v71
	ds_write_b64 v142, v[4:5] offset:15232
	global_load_dwordx4 v[36:39], v2, s[66:67] sc1 nt
	global_load_dwordx4 v[68:71], v2, s[66:67] offset:512 sc1 nt
	s_waitcnt lgkmcnt(0)
	s_barrier
	s_waitcnt lgkmcnt(0)
	s_barrier
	s_waitcnt vmcnt(31)
	v_cvt_pk_f16_f32 v4, v72, v73
	v_cvt_pk_f16_f32 v5, v74, v75
	ds_write_b64 v143, v[4:5]
	s_waitcnt vmcnt(30)
	v_cvt_pk_f16_f32 v4, v104, v105
	v_cvt_pk_f16_f32 v5, v106, v107
	ds_write_b64 v144, v[4:5]
	global_load_dwordx4 v[72:75], v2, s[52:53] offset:1024 sc1 nt
	global_load_dwordx4 v[104:107], v2, s[52:53] offset:1536 sc1 nt
	s_waitcnt vmcnt(31)
	v_cvt_pk_f16_f32 v4, v76, v77
	v_cvt_pk_f16_f32 v5, v78, v79
	ds_write_b64 v143, v[4:5] offset:2176
	s_waitcnt vmcnt(30)
	v_cvt_pk_f16_f32 v4, v108, v109
	v_cvt_pk_f16_f32 v5, v110, v111
	ds_write_b64 v144, v[4:5] offset:2176
	global_load_dwordx4 v[76:79], v2, s[54:55] offset:1024 sc1 nt
	global_load_dwordx4 v[108:111], v2, s[54:55] offset:1536 sc1 nt
	s_waitcnt vmcnt(31)
	v_cvt_pk_f16_f32 v4, v80, v81
	v_cvt_pk_f16_f32 v5, v82, v83
	ds_write_b64 v143, v[4:5] offset:4352
	s_waitcnt vmcnt(30)
	v_cvt_pk_f16_f32 v4, v112, v113
	v_cvt_pk_f16_f32 v5, v114, v115
	ds_write_b64 v144, v[4:5] offset:4352
	global_load_dwordx4 v[80:83], v2, s[56:57] offset:1024 sc1 nt
	global_load_dwordx4 v[112:115], v2, s[56:57] offset:1536 sc1 nt
	s_waitcnt vmcnt(31)
	v_cvt_pk_f16_f32 v4, v84, v85
	v_cvt_pk_f16_f32 v5, v86, v87
	ds_write_b64 v143, v[4:5] offset:6528
	s_waitcnt vmcnt(30)
	v_cvt_pk_f16_f32 v4, v116, v117
	v_cvt_pk_f16_f32 v5, v118, v119
	ds_write_b64 v144, v[4:5] offset:6528
	global_load_dwordx4 v[84:87], v2, s[58:59] offset:1024 sc1 nt
	global_load_dwordx4 v[116:119], v2, s[58:59] offset:1536 sc1 nt
	s_waitcnt vmcnt(31)
	v_cvt_pk_f16_f32 v4, v88, v89
	v_cvt_pk_f16_f32 v5, v90, v91
	ds_write_b64 v143, v[4:5] offset:8704
	s_waitcnt vmcnt(30)
	v_cvt_pk_f16_f32 v4, v120, v121
	v_cvt_pk_f16_f32 v5, v122, v123
	ds_write_b64 v144, v[4:5] offset:8704
	global_load_dwordx4 v[88:91], v2, s[60:61] offset:1024 sc1 nt
	global_load_dwordx4 v[120:123], v2, s[60:61] offset:1536 sc1 nt
	s_waitcnt vmcnt(31)
	v_cvt_pk_f16_f32 v4, v92, v93
	v_cvt_pk_f16_f32 v5, v94, v95
	ds_write_b64 v143, v[4:5] offset:10880
	s_waitcnt vmcnt(30)
	v_cvt_pk_f16_f32 v4, v124, v125
	v_cvt_pk_f16_f32 v5, v126, v127
	ds_write_b64 v144, v[4:5] offset:10880
	global_load_dwordx4 v[92:95], v2, s[62:63] offset:1024 sc1 nt
	global_load_dwordx4 v[124:127], v2, s[62:63] offset:1536 sc1 nt
	s_waitcnt vmcnt(31)
	v_cvt_pk_f16_f32 v4, v96, v97
	v_cvt_pk_f16_f32 v5, v98, v99
	ds_write_b64 v143, v[4:5] offset:13056
	s_waitcnt vmcnt(30)
	v_cvt_pk_f16_f32 v4, v128, v129
	v_cvt_pk_f16_f32 v5, v130, v131
	ds_write_b64 v144, v[4:5] offset:13056
	global_load_dwordx4 v[96:99], v2, s[64:65] offset:1024 sc1 nt
	global_load_dwordx4 v[128:131], v2, s[64:65] offset:1536 sc1 nt
	s_waitcnt vmcnt(31)
	v_cvt_pk_f16_f32 v4, v100, v101
	v_cvt_pk_f16_f32 v5, v102, v103
	ds_write_b64 v143, v[4:5] offset:15232
	s_waitcnt vmcnt(30)
	v_cvt_pk_f16_f32 v4, v132, v133
	v_cvt_pk_f16_f32 v5, v134, v135
	ds_write_b64 v144, v[4:5] offset:15232
	global_load_dwordx4 v[100:103], v2, s[66:67] offset:1024 sc1 nt
	global_load_dwordx4 v[132:135], v2, s[66:67] offset:1536 sc1 nt
	s_waitcnt lgkmcnt(0)
	s_barrier
	s_waitcnt lgkmcnt(0)
	s_barrier
	s_waitcnt vmcnt(31)
	v_cvt_pk_f16_f32 v4, v8, v9
	v_cvt_pk_f16_f32 v5, v10, v11
	ds_write_b64 v141, v[4:5]
	s_waitcnt vmcnt(30)
	v_cvt_pk_f16_f32 v4, v40, v41
	v_cvt_pk_f16_f32 v5, v42, v43
	ds_write_b64 v142, v[4:5]
	global_load_dwordx4 v[8:11], v2, s[52:53] offset:2048 sc1 nt
	global_load_dwordx4 v[40:43], v2, s[52:53] offset:2560 sc1 nt
	s_waitcnt vmcnt(31)
	v_cvt_pk_f16_f32 v4, v12, v13
	v_cvt_pk_f16_f32 v5, v14, v15
	ds_write_b64 v141, v[4:5] offset:2176
	s_waitcnt vmcnt(30)
	v_cvt_pk_f16_f32 v4, v44, v45
	v_cvt_pk_f16_f32 v5, v46, v47
	ds_write_b64 v142, v[4:5] offset:2176
	global_load_dwordx4 v[12:15], v2, s[54:55] offset:2048 sc1 nt
	global_load_dwordx4 v[44:47], v2, s[54:55] offset:2560 sc1 nt
	s_waitcnt vmcnt(31)
	v_cvt_pk_f16_f32 v4, v16, v17
	v_cvt_pk_f16_f32 v5, v18, v19
	ds_write_b64 v141, v[4:5] offset:4352
	s_waitcnt vmcnt(30)
	v_cvt_pk_f16_f32 v4, v48, v49
	v_cvt_pk_f16_f32 v5, v50, v51
	ds_write_b64 v142, v[4:5] offset:4352
	global_load_dwordx4 v[16:19], v2, s[56:57] offset:2048 sc1 nt
	global_load_dwordx4 v[48:51], v2, s[56:57] offset:2560 sc1 nt
	s_waitcnt vmcnt(31)
	v_cvt_pk_f16_f32 v4, v20, v21
	v_cvt_pk_f16_f32 v5, v22, v23
	ds_write_b64 v141, v[4:5] offset:6528
	s_waitcnt vmcnt(30)
	v_cvt_pk_f16_f32 v4, v52, v53
	v_cvt_pk_f16_f32 v5, v54, v55
	ds_write_b64 v142, v[4:5] offset:6528
	global_load_dwordx4 v[20:23], v2, s[58:59] offset:2048 sc1 nt
	global_load_dwordx4 v[52:55], v2, s[58:59] offset:2560 sc1 nt
	s_waitcnt vmcnt(31)
	v_cvt_pk_f16_f32 v4, v24, v25
	v_cvt_pk_f16_f32 v5, v26, v27
	ds_write_b64 v141, v[4:5] offset:8704
	s_waitcnt vmcnt(30)
	v_cvt_pk_f16_f32 v4, v56, v57
	v_cvt_pk_f16_f32 v5, v58, v59
	ds_write_b64 v142, v[4:5] offset:8704
	global_load_dwordx4 v[24:27], v2, s[60:61] offset:2048 sc1 nt
	global_load_dwordx4 v[56:59], v2, s[60:61] offset:2560 sc1 nt
	s_waitcnt vmcnt(31)
	v_cvt_pk_f16_f32 v4, v28, v29
	v_cvt_pk_f16_f32 v5, v30, v31
	ds_write_b64 v141, v[4:5] offset:10880
	s_waitcnt vmcnt(30)
	v_cvt_pk_f16_f32 v4, v60, v61
	v_cvt_pk_f16_f32 v5, v62, v63
	ds_write_b64 v142, v[4:5] offset:10880
	global_load_dwordx4 v[28:31], v2, s[62:63] offset:2048 sc1 nt
	global_load_dwordx4 v[60:63], v2, s[62:63] offset:2560 sc1 nt
	s_waitcnt vmcnt(31)
	v_cvt_pk_f16_f32 v4, v32, v33
	v_cvt_pk_f16_f32 v5, v34, v35
	ds_write_b64 v141, v[4:5] offset:13056
	s_waitcnt vmcnt(30)
	v_cvt_pk_f16_f32 v4, v64, v65
	v_cvt_pk_f16_f32 v5, v66, v67
	ds_write_b64 v142, v[4:5] offset:13056
	global_load_dwordx4 v[32:35], v2, s[64:65] offset:2048 sc1 nt
	global_load_dwordx4 v[64:67], v2, s[64:65] offset:2560 sc1 nt
	s_waitcnt vmcnt(31)
	v_cvt_pk_f16_f32 v4, v36, v37
	v_cvt_pk_f16_f32 v5, v38, v39
	ds_write_b64 v141, v[4:5] offset:15232
	s_waitcnt vmcnt(30)
	v_cvt_pk_f16_f32 v4, v68, v69
	v_cvt_pk_f16_f32 v5, v70, v71
	ds_write_b64 v142, v[4:5] offset:15232
	global_load_dwordx4 v[36:39], v2, s[66:67] offset:2048 sc1 nt
	global_load_dwordx4 v[68:71], v2, s[66:67] offset:2560 sc1 nt
	s_waitcnt lgkmcnt(0)
	s_barrier
	s_waitcnt lgkmcnt(0)
	s_barrier
	s_waitcnt vmcnt(31)
	v_cvt_pk_f16_f32 v4, v72, v73
	v_cvt_pk_f16_f32 v5, v74, v75
	ds_write_b64 v143, v[4:5]
	s_waitcnt vmcnt(30)
	v_cvt_pk_f16_f32 v4, v104, v105
	v_cvt_pk_f16_f32 v5, v106, v107
	ds_write_b64 v144, v[4:5]
	global_load_dwordx4 v[72:75], v2, s[52:53] offset:3072 sc1 nt
	global_load_dwordx4 v[104:107], v2, s[52:53] offset:3584 sc1 nt
	s_waitcnt vmcnt(31)
	v_cvt_pk_f16_f32 v4, v76, v77
	v_cvt_pk_f16_f32 v5, v78, v79
	ds_write_b64 v143, v[4:5] offset:2176
	s_waitcnt vmcnt(30)
	v_cvt_pk_f16_f32 v4, v108, v109
	v_cvt_pk_f16_f32 v5, v110, v111
	ds_write_b64 v144, v[4:5] offset:2176
	global_load_dwordx4 v[76:79], v2, s[54:55] offset:3072 sc1 nt
	global_load_dwordx4 v[108:111], v2, s[54:55] offset:3584 sc1 nt
	s_waitcnt vmcnt(31)
	v_cvt_pk_f16_f32 v4, v80, v81
	v_cvt_pk_f16_f32 v5, v82, v83
	ds_write_b64 v143, v[4:5] offset:4352
	s_waitcnt vmcnt(30)
	v_cvt_pk_f16_f32 v4, v112, v113
	v_cvt_pk_f16_f32 v5, v114, v115
	ds_write_b64 v144, v[4:5] offset:4352
	global_load_dwordx4 v[80:83], v2, s[56:57] offset:3072 sc1 nt
	global_load_dwordx4 v[112:115], v2, s[56:57] offset:3584 sc1 nt
	s_waitcnt vmcnt(31)
	v_cvt_pk_f16_f32 v4, v84, v85
	v_cvt_pk_f16_f32 v5, v86, v87
	ds_write_b64 v143, v[4:5] offset:6528
	s_waitcnt vmcnt(30)
	v_cvt_pk_f16_f32 v4, v116, v117
	v_cvt_pk_f16_f32 v5, v118, v119
	ds_write_b64 v144, v[4:5] offset:6528
	global_load_dwordx4 v[84:87], v2, s[58:59] offset:3072 sc1 nt
	global_load_dwordx4 v[116:119], v2, s[58:59] offset:3584 sc1 nt
	s_waitcnt vmcnt(31)
	v_cvt_pk_f16_f32 v4, v88, v89
	v_cvt_pk_f16_f32 v5, v90, v91
	ds_write_b64 v143, v[4:5] offset:8704
	s_waitcnt vmcnt(30)
	v_cvt_pk_f16_f32 v4, v120, v121
	v_cvt_pk_f16_f32 v5, v122, v123
	ds_write_b64 v144, v[4:5] offset:8704
	global_load_dwordx4 v[88:91], v2, s[60:61] offset:3072 sc1 nt
	global_load_dwordx4 v[120:123], v2, s[60:61] offset:3584 sc1 nt
	s_waitcnt vmcnt(31)
	v_cvt_pk_f16_f32 v4, v92, v93
	v_cvt_pk_f16_f32 v5, v94, v95
	ds_write_b64 v143, v[4:5] offset:10880
	s_waitcnt vmcnt(30)
	v_cvt_pk_f16_f32 v4, v124, v125
	v_cvt_pk_f16_f32 v5, v126, v127
	ds_write_b64 v144, v[4:5] offset:10880
	global_load_dwordx4 v[92:95], v2, s[62:63] offset:3072 sc1 nt
	global_load_dwordx4 v[124:127], v2, s[62:63] offset:3584 sc1 nt
	s_waitcnt vmcnt(31)
	v_cvt_pk_f16_f32 v4, v96, v97
	v_cvt_pk_f16_f32 v5, v98, v99
	ds_write_b64 v143, v[4:5] offset:13056
	s_waitcnt vmcnt(30)
	v_cvt_pk_f16_f32 v4, v128, v129
	v_cvt_pk_f16_f32 v5, v130, v131
	ds_write_b64 v144, v[4:5] offset:13056
	global_load_dwordx4 v[96:99], v2, s[64:65] offset:3072 sc1 nt
	global_load_dwordx4 v[128:131], v2, s[64:65] offset:3584 sc1 nt
	s_waitcnt vmcnt(31)
	v_cvt_pk_f16_f32 v4, v100, v101
	v_cvt_pk_f16_f32 v5, v102, v103
	ds_write_b64 v143, v[4:5] offset:15232
	s_waitcnt vmcnt(30)
	v_cvt_pk_f16_f32 v4, v132, v133
	v_cvt_pk_f16_f32 v5, v134, v135
	ds_write_b64 v144, v[4:5] offset:15232
	global_load_dwordx4 v[100:103], v2, s[66:67] offset:3072 sc1 nt
	global_load_dwordx4 v[132:135], v2, s[66:67] offset:3584 sc1 nt
	s_waitcnt lgkmcnt(0)
	s_barrier
	s_waitcnt lgkmcnt(0)
	s_barrier
	s_waitcnt vmcnt(31)
	v_cvt_pk_f16_f32 v4, v8, v9
	v_cvt_pk_f16_f32 v5, v10, v11
	ds_write_b64 v141, v[4:5]
	s_waitcnt vmcnt(30)
	v_cvt_pk_f16_f32 v4, v40, v41
	v_cvt_pk_f16_f32 v5, v42, v43
	ds_write_b64 v142, v[4:5]
	v_add_u32_e32 v2, 0x1000, v2
	global_load_dwordx4 v[8:11], v2, s[52:53] sc1 nt
	global_load_dwordx4 v[40:43], v2, s[52:53] offset:512 sc1 nt
	s_waitcnt vmcnt(31)
	v_cvt_pk_f16_f32 v4, v12, v13
	v_cvt_pk_f16_f32 v5, v14, v15
	ds_write_b64 v141, v[4:5] offset:2176
	s_waitcnt vmcnt(30)
	v_cvt_pk_f16_f32 v4, v44, v45
	v_cvt_pk_f16_f32 v5, v46, v47
	ds_write_b64 v142, v[4:5] offset:2176
	global_load_dwordx4 v[12:15], v2, s[54:55] sc1 nt
	global_load_dwordx4 v[44:47], v2, s[54:55] offset:512 sc1 nt
	s_waitcnt vmcnt(31)
	v_cvt_pk_f16_f32 v4, v16, v17
	v_cvt_pk_f16_f32 v5, v18, v19
	ds_write_b64 v141, v[4:5] offset:4352
	s_waitcnt vmcnt(30)
	v_cvt_pk_f16_f32 v4, v48, v49
	v_cvt_pk_f16_f32 v5, v50, v51
	ds_write_b64 v142, v[4:5] offset:4352
	global_load_dwordx4 v[16:19], v2, s[56:57] sc1 nt
	global_load_dwordx4 v[48:51], v2, s[56:57] offset:512 sc1 nt
	s_waitcnt vmcnt(31)
	v_cvt_pk_f16_f32 v4, v20, v21
	v_cvt_pk_f16_f32 v5, v22, v23
	ds_write_b64 v141, v[4:5] offset:6528
	s_waitcnt vmcnt(30)
	v_cvt_pk_f16_f32 v4, v52, v53
	v_cvt_pk_f16_f32 v5, v54, v55
	ds_write_b64 v142, v[4:5] offset:6528
	global_load_dwordx4 v[20:23], v2, s[58:59] sc1 nt
	global_load_dwordx4 v[52:55], v2, s[58:59] offset:512 sc1 nt
	s_waitcnt vmcnt(31)
	v_cvt_pk_f16_f32 v4, v24, v25
	v_cvt_pk_f16_f32 v5, v26, v27
	ds_write_b64 v141, v[4:5] offset:8704
	s_waitcnt vmcnt(30)
	v_cvt_pk_f16_f32 v4, v56, v57
	v_cvt_pk_f16_f32 v5, v58, v59
	ds_write_b64 v142, v[4:5] offset:8704
	global_load_dwordx4 v[24:27], v2, s[60:61] sc1 nt
	global_load_dwordx4 v[56:59], v2, s[60:61] offset:512 sc1 nt
	s_waitcnt vmcnt(31)
	v_cvt_pk_f16_f32 v4, v28, v29
	v_cvt_pk_f16_f32 v5, v30, v31
	ds_write_b64 v141, v[4:5] offset:10880
	s_waitcnt vmcnt(30)
	v_cvt_pk_f16_f32 v4, v60, v61
	v_cvt_pk_f16_f32 v5, v62, v63
	ds_write_b64 v142, v[4:5] offset:10880
	global_load_dwordx4 v[28:31], v2, s[62:63] sc1 nt
	global_load_dwordx4 v[60:63], v2, s[62:63] offset:512 sc1 nt
	s_waitcnt vmcnt(31)
	v_cvt_pk_f16_f32 v4, v32, v33
	v_cvt_pk_f16_f32 v5, v34, v35
	ds_write_b64 v141, v[4:5] offset:13056
	s_waitcnt vmcnt(30)
	v_cvt_pk_f16_f32 v4, v64, v65
	v_cvt_pk_f16_f32 v5, v66, v67
	ds_write_b64 v142, v[4:5] offset:13056
	global_load_dwordx4 v[32:35], v2, s[64:65] sc1 nt
	global_load_dwordx4 v[64:67], v2, s[64:65] offset:512 sc1 nt
	s_waitcnt vmcnt(31)
	v_cvt_pk_f16_f32 v4, v36, v37
	v_cvt_pk_f16_f32 v5, v38, v39
	ds_write_b64 v141, v[4:5] offset:15232
	s_waitcnt vmcnt(30)
	v_cvt_pk_f16_f32 v4, v68, v69
	v_cvt_pk_f16_f32 v5, v70, v71
	ds_write_b64 v142, v[4:5] offset:15232
	global_load_dwordx4 v[36:39], v2, s[66:67] sc1 nt
	global_load_dwordx4 v[68:71], v2, s[66:67] offset:512 sc1 nt
	s_waitcnt lgkmcnt(0)
	s_barrier
	s_waitcnt lgkmcnt(0)
	s_barrier
	s_waitcnt vmcnt(31)
	v_cvt_pk_f16_f32 v4, v72, v73
	v_cvt_pk_f16_f32 v5, v74, v75
	ds_write_b64 v143, v[4:5]
	s_waitcnt vmcnt(30)
	v_cvt_pk_f16_f32 v4, v104, v105
	v_cvt_pk_f16_f32 v5, v106, v107
	ds_write_b64 v144, v[4:5]
	global_load_dwordx4 v[72:75], v2, s[52:53] offset:1024 sc1 nt
	global_load_dwordx4 v[104:107], v2, s[52:53] offset:1536 sc1 nt
	s_waitcnt vmcnt(31)
	v_cvt_pk_f16_f32 v4, v76, v77
	v_cvt_pk_f16_f32 v5, v78, v79
	ds_write_b64 v143, v[4:5] offset:2176
	s_waitcnt vmcnt(30)
	v_cvt_pk_f16_f32 v4, v108, v109
	v_cvt_pk_f16_f32 v5, v110, v111
	ds_write_b64 v144, v[4:5] offset:2176
	global_load_dwordx4 v[76:79], v2, s[54:55] offset:1024 sc1 nt
	global_load_dwordx4 v[108:111], v2, s[54:55] offset:1536 sc1 nt
	s_waitcnt vmcnt(31)
	v_cvt_pk_f16_f32 v4, v80, v81
	v_cvt_pk_f16_f32 v5, v82, v83
	ds_write_b64 v143, v[4:5] offset:4352
	s_waitcnt vmcnt(30)
	v_cvt_pk_f16_f32 v4, v112, v113
	v_cvt_pk_f16_f32 v5, v114, v115
	ds_write_b64 v144, v[4:5] offset:4352
	global_load_dwordx4 v[80:83], v2, s[56:57] offset:1024 sc1 nt
	global_load_dwordx4 v[112:115], v2, s[56:57] offset:1536 sc1 nt
	s_waitcnt vmcnt(31)
	v_cvt_pk_f16_f32 v4, v84, v85
	v_cvt_pk_f16_f32 v5, v86, v87
	ds_write_b64 v143, v[4:5] offset:6528
	s_waitcnt vmcnt(30)
	v_cvt_pk_f16_f32 v4, v116, v117
	v_cvt_pk_f16_f32 v5, v118, v119
	ds_write_b64 v144, v[4:5] offset:6528
	global_load_dwordx4 v[84:87], v2, s[58:59] offset:1024 sc1 nt
	global_load_dwordx4 v[116:119], v2, s[58:59] offset:1536 sc1 nt
	s_waitcnt vmcnt(31)
	v_cvt_pk_f16_f32 v4, v88, v89
	v_cvt_pk_f16_f32 v5, v90, v91
	ds_write_b64 v143, v[4:5] offset:8704
	s_waitcnt vmcnt(30)
	v_cvt_pk_f16_f32 v4, v120, v121
	v_cvt_pk_f16_f32 v5, v122, v123
	ds_write_b64 v144, v[4:5] offset:8704
	global_load_dwordx4 v[88:91], v2, s[60:61] offset:1024 sc1 nt
	global_load_dwordx4 v[120:123], v2, s[60:61] offset:1536 sc1 nt
	s_waitcnt vmcnt(31)
	v_cvt_pk_f16_f32 v4, v92, v93
	v_cvt_pk_f16_f32 v5, v94, v95
	ds_write_b64 v143, v[4:5] offset:10880
	s_waitcnt vmcnt(30)
	v_cvt_pk_f16_f32 v4, v124, v125
	v_cvt_pk_f16_f32 v5, v126, v127
	ds_write_b64 v144, v[4:5] offset:10880
	global_load_dwordx4 v[92:95], v2, s[62:63] offset:1024 sc1 nt
	global_load_dwordx4 v[124:127], v2, s[62:63] offset:1536 sc1 nt
	s_waitcnt vmcnt(31)
	v_cvt_pk_f16_f32 v4, v96, v97
	v_cvt_pk_f16_f32 v5, v98, v99
	ds_write_b64 v143, v[4:5] offset:13056
	s_waitcnt vmcnt(30)
	v_cvt_pk_f16_f32 v4, v128, v129
	v_cvt_pk_f16_f32 v5, v130, v131
	ds_write_b64 v144, v[4:5] offset:13056
	global_load_dwordx4 v[96:99], v2, s[64:65] offset:1024 sc1 nt
	global_load_dwordx4 v[128:131], v2, s[64:65] offset:1536 sc1 nt
	s_waitcnt vmcnt(31)
	v_cvt_pk_f16_f32 v4, v100, v101
	v_cvt_pk_f16_f32 v5, v102, v103
	ds_write_b64 v143, v[4:5] offset:15232
	s_waitcnt vmcnt(30)
	v_cvt_pk_f16_f32 v4, v132, v133
	v_cvt_pk_f16_f32 v5, v134, v135
	ds_write_b64 v144, v[4:5] offset:15232
	global_load_dwordx4 v[100:103], v2, s[66:67] offset:1024 sc1 nt
	global_load_dwordx4 v[132:135], v2, s[66:67] offset:1536 sc1 nt
	s_waitcnt lgkmcnt(0)
	s_barrier
	s_waitcnt lgkmcnt(0)
	s_barrier
	s_waitcnt vmcnt(31)
	v_cvt_pk_f16_f32 v4, v8, v9
	v_cvt_pk_f16_f32 v5, v10, v11
	ds_write_b64 v141, v[4:5]
	s_waitcnt vmcnt(30)
	v_cvt_pk_f16_f32 v4, v40, v41
	v_cvt_pk_f16_f32 v5, v42, v43
	ds_write_b64 v142, v[4:5]
	global_load_dwordx4 v[8:11], v2, s[52:53] offset:2048 sc1 nt
	global_load_dwordx4 v[40:43], v2, s[52:53] offset:2560 sc1 nt
	s_waitcnt vmcnt(31)
	v_cvt_pk_f16_f32 v4, v12, v13
	v_cvt_pk_f16_f32 v5, v14, v15
	ds_write_b64 v141, v[4:5] offset:2176
	s_waitcnt vmcnt(30)
	v_cvt_pk_f16_f32 v4, v44, v45
	v_cvt_pk_f16_f32 v5, v46, v47
	ds_write_b64 v142, v[4:5] offset:2176
	global_load_dwordx4 v[12:15], v2, s[54:55] offset:2048 sc1 nt
	global_load_dwordx4 v[44:47], v2, s[54:55] offset:2560 sc1 nt
	s_waitcnt vmcnt(31)
	v_cvt_pk_f16_f32 v4, v16, v17
	v_cvt_pk_f16_f32 v5, v18, v19
	ds_write_b64 v141, v[4:5] offset:4352
	s_waitcnt vmcnt(30)
	v_cvt_pk_f16_f32 v4, v48, v49
	v_cvt_pk_f16_f32 v5, v50, v51
	ds_write_b64 v142, v[4:5] offset:4352
	global_load_dwordx4 v[16:19], v2, s[56:57] offset:2048 sc1 nt
	global_load_dwordx4 v[48:51], v2, s[56:57] offset:2560 sc1 nt
	s_waitcnt vmcnt(31)
	v_cvt_pk_f16_f32 v4, v20, v21
	v_cvt_pk_f16_f32 v5, v22, v23
	ds_write_b64 v141, v[4:5] offset:6528
	s_waitcnt vmcnt(30)
	v_cvt_pk_f16_f32 v4, v52, v53
	v_cvt_pk_f16_f32 v5, v54, v55
	ds_write_b64 v142, v[4:5] offset:6528
	global_load_dwordx4 v[20:23], v2, s[58:59] offset:2048 sc1 nt
	global_load_dwordx4 v[52:55], v2, s[58:59] offset:2560 sc1 nt
	s_waitcnt vmcnt(31)
	v_cvt_pk_f16_f32 v4, v24, v25
	v_cvt_pk_f16_f32 v5, v26, v27
	ds_write_b64 v141, v[4:5] offset:8704
	s_waitcnt vmcnt(30)
	v_cvt_pk_f16_f32 v4, v56, v57
	v_cvt_pk_f16_f32 v5, v58, v59
	ds_write_b64 v142, v[4:5] offset:8704
	global_load_dwordx4 v[24:27], v2, s[60:61] offset:2048 sc1 nt
	global_load_dwordx4 v[56:59], v2, s[60:61] offset:2560 sc1 nt
	s_waitcnt vmcnt(31)
	v_cvt_pk_f16_f32 v4, v28, v29
	v_cvt_pk_f16_f32 v5, v30, v31
	ds_write_b64 v141, v[4:5] offset:10880
	s_waitcnt vmcnt(30)
	v_cvt_pk_f16_f32 v4, v60, v61
	v_cvt_pk_f16_f32 v5, v62, v63
	ds_write_b64 v142, v[4:5] offset:10880
	global_load_dwordx4 v[28:31], v2, s[62:63] offset:2048 sc1 nt
	global_load_dwordx4 v[60:63], v2, s[62:63] offset:2560 sc1 nt
	s_waitcnt vmcnt(31)
	v_cvt_pk_f16_f32 v4, v32, v33
	v_cvt_pk_f16_f32 v5, v34, v35
	ds_write_b64 v141, v[4:5] offset:13056
	s_waitcnt vmcnt(30)
	v_cvt_pk_f16_f32 v4, v64, v65
	v_cvt_pk_f16_f32 v5, v66, v67
	ds_write_b64 v142, v[4:5] offset:13056
	global_load_dwordx4 v[32:35], v2, s[64:65] offset:2048 sc1 nt
	global_load_dwordx4 v[64:67], v2, s[64:65] offset:2560 sc1 nt
	s_waitcnt vmcnt(31)
	v_cvt_pk_f16_f32 v4, v36, v37
	v_cvt_pk_f16_f32 v5, v38, v39
	ds_write_b64 v141, v[4:5] offset:15232
	s_waitcnt vmcnt(30)
	v_cvt_pk_f16_f32 v4, v68, v69
	v_cvt_pk_f16_f32 v5, v70, v71
	ds_write_b64 v142, v[4:5] offset:15232
	global_load_dwordx4 v[36:39], v2, s[66:67] offset:2048 sc1 nt
	global_load_dwordx4 v[68:71], v2, s[66:67] offset:2560 sc1 nt
	s_waitcnt lgkmcnt(0)
	s_barrier
	s_waitcnt lgkmcnt(0)
	s_barrier
	s_waitcnt vmcnt(31)
	v_cvt_pk_f16_f32 v4, v72, v73
	v_cvt_pk_f16_f32 v5, v74, v75
	ds_write_b64 v143, v[4:5]
	s_waitcnt vmcnt(30)
	v_cvt_pk_f16_f32 v4, v104, v105
	v_cvt_pk_f16_f32 v5, v106, v107
	ds_write_b64 v144, v[4:5]
	global_load_dwordx4 v[72:75], v2, s[52:53] offset:3072 sc1 nt
	v_mov_b32_e32 v104, 0
	v_mov_b32_e32 v105, 0
	v_mov_b32_e32 v106, 0
	v_mov_b32_e32 v107, 0
	s_mov_b64 s[70:71], exec
	s_mov_b64 exec, s[68:69]
	global_load_dwordx4 v[104:107], v2, s[52:53] offset:3584 sc1 nt
	s_mov_b64 exec, s[70:71]
	s_waitcnt vmcnt(31)
	v_cvt_pk_f16_f32 v4, v76, v77
	v_cvt_pk_f16_f32 v5, v78, v79
	ds_write_b64 v143, v[4:5] offset:2176
	s_waitcnt vmcnt(30)
	v_cvt_pk_f16_f32 v4, v108, v109
	v_cvt_pk_f16_f32 v5, v110, v111
	ds_write_b64 v144, v[4:5] offset:2176
	global_load_dwordx4 v[76:79], v2, s[54:55] offset:3072 sc1 nt
	v_mov_b32_e32 v108, 0
	v_mov_b32_e32 v109, 0
	v_mov_b32_e32 v110, 0
	v_mov_b32_e32 v111, 0
	s_mov_b64 s[70:71], exec
	s_mov_b64 exec, s[68:69]
	global_load_dwordx4 v[108:111], v2, s[54:55] offset:3584 sc1 nt
	s_mov_b64 exec, s[70:71]
	s_waitcnt vmcnt(31)
	v_cvt_pk_f16_f32 v4, v80, v81
	v_cvt_pk_f16_f32 v5, v82, v83
	ds_write_b64 v143, v[4:5] offset:4352
	s_waitcnt vmcnt(30)
	v_cvt_pk_f16_f32 v4, v112, v113
	v_cvt_pk_f16_f32 v5, v114, v115
	ds_write_b64 v144, v[4:5] offset:4352
	global_load_dwordx4 v[80:83], v2, s[56:57] offset:3072 sc1 nt
	v_mov_b32_e32 v112, 0
	v_mov_b32_e32 v113, 0
	v_mov_b32_e32 v114, 0
	v_mov_b32_e32 v115, 0
	s_mov_b64 s[70:71], exec
	s_mov_b64 exec, s[68:69]
	global_load_dwordx4 v[112:115], v2, s[56:57] offset:3584 sc1 nt
	s_mov_b64 exec, s[70:71]
	s_waitcnt vmcnt(31)
	v_cvt_pk_f16_f32 v4, v84, v85
	v_cvt_pk_f16_f32 v5, v86, v87
	ds_write_b64 v143, v[4:5] offset:6528
	s_waitcnt vmcnt(30)
	v_cvt_pk_f16_f32 v4, v116, v117
	v_cvt_pk_f16_f32 v5, v118, v119
	ds_write_b64 v144, v[4:5] offset:6528
	global_load_dwordx4 v[84:87], v2, s[58:59] offset:3072 sc1 nt
	v_mov_b32_e32 v116, 0
	v_mov_b32_e32 v117, 0
	v_mov_b32_e32 v118, 0
	v_mov_b32_e32 v119, 0
	s_mov_b64 s[70:71], exec
	s_mov_b64 exec, s[68:69]
	global_load_dwordx4 v[116:119], v2, s[58:59] offset:3584 sc1 nt
	s_mov_b64 exec, s[70:71]
	s_waitcnt vmcnt(31)
	v_cvt_pk_f16_f32 v4, v88, v89
	v_cvt_pk_f16_f32 v5, v90, v91
	ds_write_b64 v143, v[4:5] offset:8704
	s_waitcnt vmcnt(30)
	v_cvt_pk_f16_f32 v4, v120, v121
	v_cvt_pk_f16_f32 v5, v122, v123
	ds_write_b64 v144, v[4:5] offset:8704
	global_load_dwordx4 v[88:91], v2, s[60:61] offset:3072 sc1 nt
	v_mov_b32_e32 v120, 0
	v_mov_b32_e32 v121, 0
	v_mov_b32_e32 v122, 0
	v_mov_b32_e32 v123, 0
	s_mov_b64 s[70:71], exec
	s_mov_b64 exec, s[68:69]
	global_load_dwordx4 v[120:123], v2, s[60:61] offset:3584 sc1 nt
	s_mov_b64 exec, s[70:71]
	s_waitcnt vmcnt(31)
	v_cvt_pk_f16_f32 v4, v92, v93
	v_cvt_pk_f16_f32 v5, v94, v95
	ds_write_b64 v143, v[4:5] offset:10880
	s_waitcnt vmcnt(30)
	v_cvt_pk_f16_f32 v4, v124, v125
	v_cvt_pk_f16_f32 v5, v126, v127
	ds_write_b64 v144, v[4:5] offset:10880
	global_load_dwordx4 v[92:95], v2, s[62:63] offset:3072 sc1 nt
	v_mov_b32_e32 v124, 0
	v_mov_b32_e32 v125, 0
	v_mov_b32_e32 v126, 0
	v_mov_b32_e32 v127, 0
	s_mov_b64 s[70:71], exec
	s_mov_b64 exec, s[68:69]
	global_load_dwordx4 v[124:127], v2, s[62:63] offset:3584 sc1 nt
	s_mov_b64 exec, s[70:71]
	s_waitcnt vmcnt(31)
	v_cvt_pk_f16_f32 v4, v96, v97
	v_cvt_pk_f16_f32 v5, v98, v99
	ds_write_b64 v143, v[4:5] offset:13056
	s_waitcnt vmcnt(30)
	v_cvt_pk_f16_f32 v4, v128, v129
	v_cvt_pk_f16_f32 v5, v130, v131
	ds_write_b64 v144, v[4:5] offset:13056
	global_load_dwordx4 v[96:99], v2, s[64:65] offset:3072 sc1 nt
	v_mov_b32_e32 v128, 0
	v_mov_b32_e32 v129, 0
	v_mov_b32_e32 v130, 0
	v_mov_b32_e32 v131, 0
	s_mov_b64 s[70:71], exec
	s_mov_b64 exec, s[68:69]
	global_load_dwordx4 v[128:131], v2, s[64:65] offset:3584 sc1 nt
	s_mov_b64 exec, s[70:71]
	s_waitcnt vmcnt(31)
	v_cvt_pk_f16_f32 v4, v100, v101
	v_cvt_pk_f16_f32 v5, v102, v103
	ds_write_b64 v143, v[4:5] offset:15232
	s_waitcnt vmcnt(30)
	v_cvt_pk_f16_f32 v4, v132, v133
	v_cvt_pk_f16_f32 v5, v134, v135
	ds_write_b64 v144, v[4:5] offset:15232
	global_load_dwordx4 v[100:103], v2, s[66:67] offset:3072 sc1 nt
	v_mov_b32_e32 v132, 0
	v_mov_b32_e32 v133, 0
	v_mov_b32_e32 v134, 0
	v_mov_b32_e32 v135, 0
	s_mov_b64 s[70:71], exec
	s_mov_b64 exec, s[68:69]
	global_load_dwordx4 v[132:135], v2, s[66:67] offset:3584 sc1 nt
	s_mov_b64 exec, s[70:71]
	s_waitcnt lgkmcnt(0)
	s_barrier
	s_waitcnt lgkmcnt(0)
	s_barrier
	s_waitcnt vmcnt(31)
	v_cvt_pk_f16_f32 v4, v8, v9
	v_cvt_pk_f16_f32 v5, v10, v11
	ds_write_b64 v141, v[4:5]
	s_waitcnt vmcnt(30)
	v_cvt_pk_f16_f32 v4, v40, v41
	v_cvt_pk_f16_f32 v5, v42, v43
	ds_write_b64 v142, v[4:5]
	s_waitcnt vmcnt(29)
	v_cvt_pk_f16_f32 v4, v12, v13
	v_cvt_pk_f16_f32 v5, v14, v15
	ds_write_b64 v141, v[4:5] offset:2176
	s_waitcnt vmcnt(28)
	v_cvt_pk_f16_f32 v4, v44, v45
	v_cvt_pk_f16_f32 v5, v46, v47
	ds_write_b64 v142, v[4:5] offset:2176
	s_waitcnt vmcnt(27)
	v_cvt_pk_f16_f32 v4, v16, v17
	v_cvt_pk_f16_f32 v5, v18, v19
	ds_write_b64 v141, v[4:5] offset:4352
	s_waitcnt vmcnt(26)
	v_cvt_pk_f16_f32 v4, v48, v49
	v_cvt_pk_f16_f32 v5, v50, v51
	ds_write_b64 v142, v[4:5] offset:4352
	s_waitcnt vmcnt(25)
	v_cvt_pk_f16_f32 v4, v20, v21
	v_cvt_pk_f16_f32 v5, v22, v23
	ds_write_b64 v141, v[4:5] offset:6528
	s_waitcnt vmcnt(24)
	v_cvt_pk_f16_f32 v4, v52, v53
	v_cvt_pk_f16_f32 v5, v54, v55
	ds_write_b64 v142, v[4:5] offset:6528
	s_waitcnt vmcnt(23)
	v_cvt_pk_f16_f32 v4, v24, v25
	v_cvt_pk_f16_f32 v5, v26, v27
	ds_write_b64 v141, v[4:5] offset:8704
	s_waitcnt vmcnt(22)
	v_cvt_pk_f16_f32 v4, v56, v57
	v_cvt_pk_f16_f32 v5, v58, v59
	ds_write_b64 v142, v[4:5] offset:8704
	s_waitcnt vmcnt(21)
	v_cvt_pk_f16_f32 v4, v28, v29
	v_cvt_pk_f16_f32 v5, v30, v31
	ds_write_b64 v141, v[4:5] offset:10880
	s_waitcnt vmcnt(20)
	v_cvt_pk_f16_f32 v4, v60, v61
	v_cvt_pk_f16_f32 v5, v62, v63
	ds_write_b64 v142, v[4:5] offset:10880
	s_waitcnt vmcnt(19)
	v_cvt_pk_f16_f32 v4, v32, v33
	v_cvt_pk_f16_f32 v5, v34, v35
	ds_write_b64 v141, v[4:5] offset:13056
	s_waitcnt vmcnt(18)
	v_cvt_pk_f16_f32 v4, v64, v65
	v_cvt_pk_f16_f32 v5, v66, v67
	ds_write_b64 v142, v[4:5] offset:13056
	s_waitcnt vmcnt(17)
	v_cvt_pk_f16_f32 v4, v36, v37
	v_cvt_pk_f16_f32 v5, v38, v39
	ds_write_b64 v141, v[4:5] offset:15232
	s_waitcnt vmcnt(16)
	v_cvt_pk_f16_f32 v4, v68, v69
	v_cvt_pk_f16_f32 v5, v70, v71
	ds_write_b64 v142, v[4:5] offset:15232
	s_waitcnt lgkmcnt(0)
	s_barrier
	s_waitcnt lgkmcnt(0)
	s_barrier
	s_waitcnt vmcnt(15)
	v_cvt_pk_f16_f32 v4, v72, v73
	v_cvt_pk_f16_f32 v5, v74, v75
	ds_write_b64 v143, v[4:5]
	s_waitcnt vmcnt(14)
	v_cvt_pk_f16_f32 v4, v104, v105
	v_cvt_pk_f16_f32 v5, v106, v107
	s_mov_b64 s[70:71], exec
	s_mov_b64 exec, s[78:79]
	ds_write_b64 v144, v[4:5]
	s_mov_b64 exec, s[70:71]
	s_waitcnt vmcnt(13)
	v_cvt_pk_f16_f32 v4, v76, v77
	v_cvt_pk_f16_f32 v5, v78, v79
	ds_write_b64 v143, v[4:5] offset:2176
	s_waitcnt vmcnt(12)
	v_cvt_pk_f16_f32 v4, v108, v109
	v_cvt_pk_f16_f32 v5, v110, v111
	s_mov_b64 s[70:71], exec
	s_mov_b64 exec, s[78:79]
	ds_write_b64 v144, v[4:5] offset:2176
	s_mov_b64 exec, s[70:71]
	s_waitcnt vmcnt(11)
	v_cvt_pk_f16_f32 v4, v80, v81
	v_cvt_pk_f16_f32 v5, v82, v83
	ds_write_b64 v143, v[4:5] offset:4352
	s_waitcnt vmcnt(10)
	v_cvt_pk_f16_f32 v4, v112, v113
	v_cvt_pk_f16_f32 v5, v114, v115
	s_mov_b64 s[70:71], exec
	s_mov_b64 exec, s[78:79]
	ds_write_b64 v144, v[4:5] offset:4352
	s_mov_b64 exec, s[70:71]
	s_waitcnt vmcnt(9)
	v_cvt_pk_f16_f32 v4, v84, v85
	v_cvt_pk_f16_f32 v5, v86, v87
	ds_write_b64 v143, v[4:5] offset:6528
	s_waitcnt vmcnt(8)
	v_cvt_pk_f16_f32 v4, v116, v117
	v_cvt_pk_f16_f32 v5, v118, v119
	s_mov_b64 s[70:71], exec
	s_mov_b64 exec, s[78:79]
	ds_write_b64 v144, v[4:5] offset:6528
	s_mov_b64 exec, s[70:71]
	s_waitcnt vmcnt(7)
	v_cvt_pk_f16_f32 v4, v88, v89
	v_cvt_pk_f16_f32 v5, v90, v91
	ds_write_b64 v143, v[4:5] offset:8704
	s_waitcnt vmcnt(6)
	v_cvt_pk_f16_f32 v4, v120, v121
	v_cvt_pk_f16_f32 v5, v122, v123
	s_mov_b64 s[70:71], exec
	s_mov_b64 exec, s[78:79]
	ds_write_b64 v144, v[4:5] offset:8704
	s_mov_b64 exec, s[70:71]
	s_waitcnt vmcnt(5)
	v_cvt_pk_f16_f32 v4, v92, v93
	v_cvt_pk_f16_f32 v5, v94, v95
	ds_write_b64 v143, v[4:5] offset:10880
	s_waitcnt vmcnt(4)
	v_cvt_pk_f16_f32 v4, v124, v125
	v_cvt_pk_f16_f32 v5, v126, v127
	s_mov_b64 s[70:71], exec
	s_mov_b64 exec, s[78:79]
	ds_write_b64 v144, v[4:5] offset:10880
	s_mov_b64 exec, s[70:71]
	s_waitcnt vmcnt(3)
	v_cvt_pk_f16_f32 v4, v96, v97
	v_cvt_pk_f16_f32 v5, v98, v99
	ds_write_b64 v143, v[4:5] offset:13056
	s_waitcnt vmcnt(2)
	v_cvt_pk_f16_f32 v4, v128, v129
	v_cvt_pk_f16_f32 v5, v130, v131
	s_mov_b64 s[70:71], exec
	s_mov_b64 exec, s[78:79]
	ds_write_b64 v144, v[4:5] offset:13056
	s_mov_b64 exec, s[70:71]
	s_waitcnt vmcnt(1)
	v_cvt_pk_f16_f32 v4, v100, v101
	v_cvt_pk_f16_f32 v5, v102, v103
	ds_write_b64 v143, v[4:5] offset:15232
	s_waitcnt vmcnt(0)
	v_cvt_pk_f16_f32 v4, v132, v133
	v_cvt_pk_f16_f32 v5, v134, v135
	s_mov_b64 s[70:71], exec
	s_mov_b64 exec, s[78:79]
	ds_write_b64 v144, v[4:5] offset:15232
	s_mov_b64 exec, s[70:71]
	s_waitcnt lgkmcnt(0)
	s_barrier
	s_waitcnt lgkmcnt(0)
	s_barrier
	s_barrier
	s_barrier
	s_endpgm
